# moe_up_lds: MoE up epilogue stages e4m3 outputs through LDS scratch, full 128B-line dwordx4 sc1 stores
# speedup vs baseline: 1.0166x; 1.0034x over previous
.LBB0_1945:
	s_ashr_i32 s2, s10, 3
	s_ashr_i32 s3, s2, 31
	s_lshl_b64 s[2:3], s[2:3], 13
	s_add_u32 s2, s75, s2
	s_addc_u32 s3, s78, s3
	s_lshl_b64 s[0:1], s[0:1], 2
	s_add_u32 s0, s2, s0
	s_addc_u32 s1, s3, s1
	s_lshl_b32 s2, s24, 2
	s_add_u32 s0, s0, s2
	s_addc_u32 s1, s1, 0
	v_ashrrev_i32_e32 v31, 31, v30
	s_mov_b32 s2, 0xc0c00000
	s_lshl_b32 s0, s7, 7
	s_ashr_i32 s1, s0, 31
	s_mov_b32 s72, s6
	s_waitcnt vmcnt(12)
	v_mov_b32_dpp v4, v1 row_newbcast:4 row_mask:0xf bank_mask:0xf
	v_mov_b32_dpp v5, v1 row_newbcast:5 row_mask:0xf bank_mask:0xf
	v_mov_b32_dpp v6, v1 row_newbcast:6 row_mask:0xf bank_mask:0xf
	v_mov_b32_dpp v7, v1 row_newbcast:7 row_mask:0xf bank_mask:0xf
	v_mov_b32_dpp v8, v1 row_newbcast:0 row_mask:0xf bank_mask:0xf
	v_mov_b32_dpp v9, v1 row_newbcast:1 row_mask:0xf bank_mask:0xf
	v_mov_b32_dpp v10, v1 row_newbcast:2 row_mask:0xf bank_mask:0xf
	v_mov_b32_dpp v11, v1 row_newbcast:3 row_mask:0xf bank_mask:0xf
	v_mov_b32_dpp v22, v1 row_newbcast:12 row_mask:0xf bank_mask:0xf
	v_mov_b32_dpp v23, v1 row_newbcast:13 row_mask:0xf bank_mask:0xf
	v_mov_b32_dpp v24, v1 row_newbcast:14 row_mask:0xf bank_mask:0xf
	v_mov_b32_dpp v25, v1 row_newbcast:15 row_mask:0xf bank_mask:0xf
	v_mov_b32_dpp v32, v1 row_newbcast:8 row_mask:0xf bank_mask:0xf
	v_mov_b32_dpp v33, v1 row_newbcast:9 row_mask:0xf bank_mask:0xf
	v_mov_b32_dpp v34, v1 row_newbcast:10 row_mask:0xf bank_mask:0xf
	v_mov_b32_dpp v35, v1 row_newbcast:11 row_mask:0xf bank_mask:0xf
	v_pk_add_f32 v[20:21], v[24:25], 1.0 op_sel_hi:[1,0]
	v_pk_add_f32 v[26:27], v[34:35], 1.0 op_sel_hi:[1,0]
	v_pk_add_f32 v[32:33], v[32:33], 1.0 op_sel_hi:[1,0]
	v_pk_add_f32 v[22:23], v[22:23], 1.0 op_sel_hi:[1,0]
	v_and_b32_e32 v60, 15, v0
	v_lshrrev_b32_e32 v61, 6, v0
	v_lshrrev_b32_e32 v62, 2, v61
	v_lshl_add_u32 v60, v62, 4, v60
	v_mul_u32_u24_e32 v60, 0x90, v60
	v_and_b32_e32 v62, 3, v61
	v_lshl_add_u32 v60, v62, 5, v60
	v_bfe_u32 v62, v0, 4, 2
	v_lshl_add_u32 v60, v62, 3, v60
	v_add_u32_e32 v60, 0x20400, v60
	v_and_b32_e32 v62, 0xff, v0
	v_lshrrev_b32_e32 v63, 3, v62
	v_and_b32_e32 v62, 7, v62
	v_mul_u32_u24_e32 v61, 0x90, v63
	v_lshl_add_u32 v61, v62, 4, v61
	v_add_u32_e32 v61, 0x20400, v61
	v_lshrrev_b32_e32 v64, 4, v63
	v_and_b32_e32 v63, 15, v63
	v_lshl_add_u32 v63, v64, 6, v63
	v_lshlrev_b32_e32 v63, 10, v63
	v_lshl_add_u32 v56, v62, 4, v63
	v_mov_b32_e32 v57, 0
	s_lshl_b32 s98, s8, 18
	s_add_u32 s98, s14, s98
	s_addc_u32 s99, s15, 0
	s_add_u32 s98, s98, s0
	s_addc_u32 s99, s99, 0
	v_lshl_add_u64 v[56:57], s[98:99], 0, v[56:57]
	v_readfirstlane_b32 s98, v0
	s_lshr_b32 s98, s98, 8
	s_mov_b32 s100, 0x3c800000
	s_mov_b32 s101, 0xc01d265f
	s_mov_b64 s[0:1], 0x4000
	v_pk_fma_f32 v[34:35], v[196:197], s[100:101], v[8:9] op_sel_hi:[1,0,1]
	v_pk_fma_f32 v[36:37], v[198:199], s[100:101], v[10:11] op_sel_hi:[1,0,1]
	v_min_f32_e32 v34, 0x40e00000, v34
	v_min_f32_e32 v35, 0x40e00000, v35
	v_min_f32_e32 v36, 0x40e00000, v36
	v_min_f32_e32 v37, 0x40e00000, v37
	v_pk_mul_f32 v[38:39], v[34:35], s[100:101] op_sel:[0,1] op_sel_hi:[1,1]
	v_pk_mul_f32 v[40:41], v[36:37], s[100:101] op_sel:[0,1] op_sel_hi:[1,1]
	v_exp_f32_e32 v38, v38
	v_exp_f32_e32 v39, v39
	v_exp_f32_e32 v40, v40
	v_exp_f32_e32 v41, v41
	v_pk_fma_f32 v[42:43], v[164:165], s[100:101], v[32:33] op_sel_hi:[1,0,1]
	v_pk_fma_f32 v[44:45], v[166:167], s[100:101], v[26:27] op_sel_hi:[1,0,1]
	v_pk_add_f32 v[38:39], v[38:39], 1.0 op_sel_hi:[1,0]
	v_pk_add_f32 v[40:41], v[40:41], 1.0 op_sel_hi:[1,0]
	v_rcp_f32_e32 v38, v38
	v_rcp_f32_e32 v39, v39
	v_rcp_f32_e32 v40, v40
	v_rcp_f32_e32 v41, v41
	v_med3_f32 v42, v42, s2, v250
	v_med3_f32 v43, v43, s2, v250
	v_med3_f32 v44, v44, s2, v250
	v_med3_f32 v45, v45, s2, v250
	v_pk_mul_f32 v[34:35], v[34:35], v[38:39]
	v_pk_mul_f32 v[36:37], v[36:37], v[40:41]
	v_pk_mul_f32 v[48:49], v[42:43], v[34:35]
	v_pk_mul_f32 v[50:51], v[44:45], v[36:37]
	v_pk_fma_f32 v[34:35], v[192:193], s[100:101], v[4:5] op_sel_hi:[1,0,1]
	v_pk_fma_f32 v[36:37], v[194:195], s[100:101], v[6:7] op_sel_hi:[1,0,1]
	v_min_f32_e32 v34, 0x40e00000, v34
	v_min_f32_e32 v35, 0x40e00000, v35
	v_min_f32_e32 v36, 0x40e00000, v36
	v_min_f32_e32 v37, 0x40e00000, v37
	v_pk_mul_f32 v[38:39], v[34:35], s[100:101] op_sel:[0,1] op_sel_hi:[1,1]
	v_pk_mul_f32 v[40:41], v[36:37], s[100:101] op_sel:[0,1] op_sel_hi:[1,1]
	v_exp_f32_e32 v38, v38
	v_exp_f32_e32 v39, v39
	v_exp_f32_e32 v40, v40
	v_exp_f32_e32 v41, v41
	v_pk_fma_f32 v[42:43], v[160:161], s[100:101], v[22:23] op_sel_hi:[1,0,1]
	v_pk_fma_f32 v[44:45], v[162:163], s[100:101], v[20:21] op_sel_hi:[1,0,1]
	v_pk_add_f32 v[38:39], v[38:39], 1.0 op_sel_hi:[1,0]
	v_pk_add_f32 v[40:41], v[40:41], 1.0 op_sel_hi:[1,0]
	v_rcp_f32_e32 v38, v38
	v_rcp_f32_e32 v39, v39
	v_rcp_f32_e32 v40, v40
	v_rcp_f32_e32 v41, v41
	v_med3_f32 v42, v42, s2, v250
	v_med3_f32 v43, v43, s2, v250
	v_med3_f32 v44, v44, s2, v250
	v_med3_f32 v45, v45, s2, v250
	v_pk_mul_f32 v[34:35], v[34:35], v[38:39]
	v_pk_mul_f32 v[36:37], v[36:37], v[40:41]
	v_pk_mul_f32 v[52:53], v[42:43], v[34:35]
	v_pk_mul_f32 v[54:55], v[44:45], v[36:37]
	v_cvt_pk_fp8_f32 v46, v48, v49
	v_cvt_pk_fp8_f32 v46, v50, v51 op_sel:[0,0,1]
	v_cvt_pk_fp8_f32 v47, v52, v53
	v_cvt_pk_fp8_f32 v47, v54, v55 op_sel:[0,0,1]
	ds_write_b64 v60, v[46:47]
	s_waitcnt lgkmcnt(0)
	s_barrier
	s_cmp_lg_u32 s98, 0
	s_cbranch_scc1 .Lupl_skip_0
	ds_read_b128 v[64:67], v61
	s_waitcnt lgkmcnt(0)
	global_store_dwordx4 v[56:57], v[64:67], off sc1
.Lupl_skip_0:
	v_lshl_add_u64 v[56:57], v[56:57], 0, s[0:1]
	v_pk_fma_f32 v[34:35], v[188:189], s[100:101], v[8:9] op_sel_hi:[1,0,1]
	v_pk_fma_f32 v[36:37], v[190:191], s[100:101], v[10:11] op_sel_hi:[1,0,1]
	v_min_f32_e32 v34, 0x40e00000, v34
	v_min_f32_e32 v35, 0x40e00000, v35
	v_min_f32_e32 v36, 0x40e00000, v36
	v_min_f32_e32 v37, 0x40e00000, v37
	v_pk_mul_f32 v[38:39], v[34:35], s[100:101] op_sel:[0,1] op_sel_hi:[1,1]
	v_pk_mul_f32 v[40:41], v[36:37], s[100:101] op_sel:[0,1] op_sel_hi:[1,1]
	v_exp_f32_e32 v38, v38
	v_exp_f32_e32 v39, v39
	v_exp_f32_e32 v40, v40
	v_exp_f32_e32 v41, v41
	v_pk_fma_f32 v[42:43], v[156:157], s[100:101], v[32:33] op_sel_hi:[1,0,1]
	v_pk_fma_f32 v[44:45], v[158:159], s[100:101], v[26:27] op_sel_hi:[1,0,1]
	v_pk_add_f32 v[38:39], v[38:39], 1.0 op_sel_hi:[1,0]
	v_pk_add_f32 v[40:41], v[40:41], 1.0 op_sel_hi:[1,0]
	v_rcp_f32_e32 v38, v38
	v_rcp_f32_e32 v39, v39
	v_rcp_f32_e32 v40, v40
	v_rcp_f32_e32 v41, v41
	v_med3_f32 v42, v42, s2, v250
	v_med3_f32 v43, v43, s2, v250
	v_med3_f32 v44, v44, s2, v250
	v_med3_f32 v45, v45, s2, v250
	v_pk_mul_f32 v[34:35], v[34:35], v[38:39]
	v_pk_mul_f32 v[36:37], v[36:37], v[40:41]
	v_pk_mul_f32 v[48:49], v[42:43], v[34:35]
	v_pk_mul_f32 v[50:51], v[44:45], v[36:37]
	v_pk_fma_f32 v[34:35], v[184:185], s[100:101], v[4:5] op_sel_hi:[1,0,1]
	v_pk_fma_f32 v[36:37], v[186:187], s[100:101], v[6:7] op_sel_hi:[1,0,1]
	v_min_f32_e32 v34, 0x40e00000, v34
	v_min_f32_e32 v35, 0x40e00000, v35
	v_min_f32_e32 v36, 0x40e00000, v36
	v_min_f32_e32 v37, 0x40e00000, v37
	v_pk_mul_f32 v[38:39], v[34:35], s[100:101] op_sel:[0,1] op_sel_hi:[1,1]
	v_pk_mul_f32 v[40:41], v[36:37], s[100:101] op_sel:[0,1] op_sel_hi:[1,1]
	v_exp_f32_e32 v38, v38
	v_exp_f32_e32 v39, v39
	v_exp_f32_e32 v40, v40
	v_exp_f32_e32 v41, v41
	v_pk_fma_f32 v[42:43], v[152:153], s[100:101], v[22:23] op_sel_hi:[1,0,1]
	v_pk_fma_f32 v[44:45], v[154:155], s[100:101], v[20:21] op_sel_hi:[1,0,1]
	v_pk_add_f32 v[38:39], v[38:39], 1.0 op_sel_hi:[1,0]
	v_pk_add_f32 v[40:41], v[40:41], 1.0 op_sel_hi:[1,0]
	v_rcp_f32_e32 v38, v38
	v_rcp_f32_e32 v39, v39
	v_rcp_f32_e32 v40, v40
	v_rcp_f32_e32 v41, v41
	v_med3_f32 v42, v42, s2, v250
	v_med3_f32 v43, v43, s2, v250
	v_med3_f32 v44, v44, s2, v250
	v_med3_f32 v45, v45, s2, v250
	v_pk_mul_f32 v[34:35], v[34:35], v[38:39]
	v_pk_mul_f32 v[36:37], v[36:37], v[40:41]
	v_pk_mul_f32 v[52:53], v[42:43], v[34:35]
	v_pk_mul_f32 v[54:55], v[44:45], v[36:37]
	v_cvt_pk_fp8_f32 v58, v48, v49
	v_cvt_pk_fp8_f32 v58, v50, v51 op_sel:[0,0,1]
	v_cvt_pk_fp8_f32 v59, v52, v53
	v_cvt_pk_fp8_f32 v59, v54, v55 op_sel:[0,0,1]
	ds_write_b64 v60, v[58:59] offset:4608
	s_waitcnt lgkmcnt(0)
	s_barrier
	s_cmp_lg_u32 s98, 1
	s_cbranch_scc1 .Lupl_skip_1
	ds_read_b128 v[64:67], v61 offset:4608
	s_waitcnt lgkmcnt(0)
	global_store_dwordx4 v[56:57], v[64:67], off sc1
.Lupl_skip_1:
	v_lshl_add_u64 v[56:57], v[56:57], 0, s[0:1]
	v_pk_fma_f32 v[34:35], v[180:181], s[100:101], v[8:9] op_sel_hi:[1,0,1]
	v_pk_fma_f32 v[36:37], v[182:183], s[100:101], v[10:11] op_sel_hi:[1,0,1]
	v_min_f32_e32 v34, 0x40e00000, v34
	v_min_f32_e32 v35, 0x40e00000, v35
	v_min_f32_e32 v36, 0x40e00000, v36
	v_min_f32_e32 v37, 0x40e00000, v37
	v_pk_mul_f32 v[38:39], v[34:35], s[100:101] op_sel:[0,1] op_sel_hi:[1,1]
	v_pk_mul_f32 v[40:41], v[36:37], s[100:101] op_sel:[0,1] op_sel_hi:[1,1]
	v_exp_f32_e32 v38, v38
	v_exp_f32_e32 v39, v39
	v_exp_f32_e32 v40, v40
	v_exp_f32_e32 v41, v41
	v_pk_fma_f32 v[42:43], v[148:149], s[100:101], v[32:33] op_sel_hi:[1,0,1]
	v_pk_fma_f32 v[44:45], v[150:151], s[100:101], v[26:27] op_sel_hi:[1,0,1]
	v_pk_add_f32 v[38:39], v[38:39], 1.0 op_sel_hi:[1,0]
	v_pk_add_f32 v[40:41], v[40:41], 1.0 op_sel_hi:[1,0]
	v_rcp_f32_e32 v38, v38
	v_rcp_f32_e32 v39, v39
	v_rcp_f32_e32 v40, v40
	v_rcp_f32_e32 v41, v41
	v_med3_f32 v42, v42, s2, v250
	v_med3_f32 v43, v43, s2, v250
	v_med3_f32 v44, v44, s2, v250
	v_med3_f32 v45, v45, s2, v250
	v_pk_mul_f32 v[34:35], v[34:35], v[38:39]
	v_pk_mul_f32 v[36:37], v[36:37], v[40:41]
	v_pk_mul_f32 v[48:49], v[42:43], v[34:35]
	v_pk_mul_f32 v[50:51], v[44:45], v[36:37]
	v_pk_fma_f32 v[34:35], v[176:177], s[100:101], v[4:5] op_sel_hi:[1,0,1]
	v_pk_fma_f32 v[36:37], v[178:179], s[100:101], v[6:7] op_sel_hi:[1,0,1]
	v_min_f32_e32 v34, 0x40e00000, v34
	v_min_f32_e32 v35, 0x40e00000, v35
	v_min_f32_e32 v36, 0x40e00000, v36
	v_min_f32_e32 v37, 0x40e00000, v37
	v_pk_mul_f32 v[38:39], v[34:35], s[100:101] op_sel:[0,1] op_sel_hi:[1,1]
	v_pk_mul_f32 v[40:41], v[36:37], s[100:101] op_sel:[0,1] op_sel_hi:[1,1]
	v_exp_f32_e32 v38, v38
	v_exp_f32_e32 v39, v39
	v_exp_f32_e32 v40, v40
	v_exp_f32_e32 v41, v41
	v_pk_fma_f32 v[42:43], v[144:145], s[100:101], v[22:23] op_sel_hi:[1,0,1]
	v_pk_fma_f32 v[44:45], v[146:147], s[100:101], v[20:21] op_sel_hi:[1,0,1]
	v_pk_add_f32 v[38:39], v[38:39], 1.0 op_sel_hi:[1,0]
	v_pk_add_f32 v[40:41], v[40:41], 1.0 op_sel_hi:[1,0]
	v_rcp_f32_e32 v38, v38
	v_rcp_f32_e32 v39, v39
	v_rcp_f32_e32 v40, v40
	v_rcp_f32_e32 v41, v41
	v_med3_f32 v42, v42, s2, v250
	v_med3_f32 v43, v43, s2, v250
	v_med3_f32 v44, v44, s2, v250
	v_med3_f32 v45, v45, s2, v250
	v_pk_mul_f32 v[34:35], v[34:35], v[38:39]
	v_pk_mul_f32 v[36:37], v[36:37], v[40:41]
	v_pk_mul_f32 v[52:53], v[42:43], v[34:35]
	v_pk_mul_f32 v[54:55], v[44:45], v[36:37]
	v_cvt_pk_fp8_f32 v46, v48, v49
	v_cvt_pk_fp8_f32 v46, v50, v51 op_sel:[0,0,1]
	v_cvt_pk_fp8_f32 v47, v52, v53
	v_cvt_pk_fp8_f32 v47, v54, v55 op_sel:[0,0,1]
	ds_write_b64 v60, v[46:47]
	s_waitcnt lgkmcnt(0)
	s_barrier
	s_cmp_lg_u32 s98, 0
	s_cbranch_scc1 .Lupl_skip_2
	ds_read_b128 v[64:67], v61
	s_waitcnt lgkmcnt(0)
	global_store_dwordx4 v[56:57], v[64:67], off sc1
.Lupl_skip_2:
	v_lshl_add_u64 v[56:57], v[56:57], 0, s[0:1]
	v_pk_fma_f32 v[34:35], v[172:173], s[100:101], v[8:9] op_sel_hi:[1,0,1]
	v_pk_fma_f32 v[36:37], v[174:175], s[100:101], v[10:11] op_sel_hi:[1,0,1]
	v_min_f32_e32 v34, 0x40e00000, v34
	v_min_f32_e32 v35, 0x40e00000, v35
	v_min_f32_e32 v36, 0x40e00000, v36
	v_min_f32_e32 v37, 0x40e00000, v37
	v_pk_mul_f32 v[38:39], v[34:35], s[100:101] op_sel:[0,1] op_sel_hi:[1,1]
	v_pk_mul_f32 v[40:41], v[36:37], s[100:101] op_sel:[0,1] op_sel_hi:[1,1]
	v_exp_f32_e32 v38, v38
	v_exp_f32_e32 v39, v39
	v_exp_f32_e32 v40, v40
	v_exp_f32_e32 v41, v41
	v_pk_fma_f32 v[42:43], v[140:141], s[100:101], v[32:33] op_sel_hi:[1,0,1]
	v_pk_fma_f32 v[44:45], v[142:143], s[100:101], v[26:27] op_sel_hi:[1,0,1]
	v_pk_add_f32 v[38:39], v[38:39], 1.0 op_sel_hi:[1,0]
	v_pk_add_f32 v[40:41], v[40:41], 1.0 op_sel_hi:[1,0]
	v_rcp_f32_e32 v38, v38
	v_rcp_f32_e32 v39, v39
	v_rcp_f32_e32 v40, v40
	v_rcp_f32_e32 v41, v41
	v_med3_f32 v42, v42, s2, v250
	v_med3_f32 v43, v43, s2, v250
	v_med3_f32 v44, v44, s2, v250
	v_med3_f32 v45, v45, s2, v250
	v_pk_mul_f32 v[34:35], v[34:35], v[38:39]
	v_pk_mul_f32 v[36:37], v[36:37], v[40:41]
	v_pk_mul_f32 v[48:49], v[42:43], v[34:35]
	v_pk_mul_f32 v[50:51], v[44:45], v[36:37]
	v_pk_fma_f32 v[34:35], v[168:169], s[100:101], v[4:5] op_sel_hi:[1,0,1]
	v_pk_fma_f32 v[36:37], v[170:171], s[100:101], v[6:7] op_sel_hi:[1,0,1]
	v_min_f32_e32 v34, 0x40e00000, v34
	v_min_f32_e32 v35, 0x40e00000, v35
	v_min_f32_e32 v36, 0x40e00000, v36
	v_min_f32_e32 v37, 0x40e00000, v37
	v_pk_mul_f32 v[38:39], v[34:35], s[100:101] op_sel:[0,1] op_sel_hi:[1,1]
	v_pk_mul_f32 v[40:41], v[36:37], s[100:101] op_sel:[0,1] op_sel_hi:[1,1]
	v_exp_f32_e32 v38, v38
	v_exp_f32_e32 v39, v39
	v_exp_f32_e32 v40, v40
	v_exp_f32_e32 v41, v41
	v_pk_fma_f32 v[42:43], v[136:137], s[100:101], v[22:23] op_sel_hi:[1,0,1]
	v_pk_fma_f32 v[44:45], v[138:139], s[100:101], v[20:21] op_sel_hi:[1,0,1]
	v_pk_add_f32 v[38:39], v[38:39], 1.0 op_sel_hi:[1,0]
	v_pk_add_f32 v[40:41], v[40:41], 1.0 op_sel_hi:[1,0]
	v_rcp_f32_e32 v38, v38
	v_rcp_f32_e32 v39, v39
	v_rcp_f32_e32 v40, v40
	v_rcp_f32_e32 v41, v41
	v_med3_f32 v42, v42, s2, v250
	v_med3_f32 v43, v43, s2, v250
	v_med3_f32 v44, v44, s2, v250
	v_med3_f32 v45, v45, s2, v250
	v_pk_mul_f32 v[34:35], v[34:35], v[38:39]
	v_pk_mul_f32 v[36:37], v[36:37], v[40:41]
	v_pk_mul_f32 v[52:53], v[42:43], v[34:35]
	v_pk_mul_f32 v[54:55], v[44:45], v[36:37]
	v_cvt_pk_fp8_f32 v58, v48, v49
	v_cvt_pk_fp8_f32 v58, v50, v51 op_sel:[0,0,1]
	v_cvt_pk_fp8_f32 v59, v52, v53
	v_cvt_pk_fp8_f32 v59, v54, v55 op_sel:[0,0,1]
	ds_write_b64 v60, v[58:59] offset:4608
	s_waitcnt lgkmcnt(0)
	s_barrier
	s_cmp_lg_u32 s98, 1
	s_cbranch_scc1 .Lupl_skip_3
	ds_read_b128 v[64:67], v61 offset:4608
	s_waitcnt lgkmcnt(0)
	global_store_dwordx4 v[56:57], v[64:67], off sc1
.Lupl_skip_3:
	v_lshl_add_u64 v[56:57], v[56:57], 0, s[0:1]
	v_lshl_add_u64 v[56:57], v[56:57], 0, s[0:1]
	v_lshl_add_u64 v[56:57], v[56:57], 0, s[0:1]
	v_lshl_add_u64 v[56:57], v[56:57], 0, s[0:1]
	v_lshl_add_u64 v[56:57], v[56:57], 0, s[0:1]
	v_pk_fma_f32 v[34:35], v[132:133], s[100:101], v[8:9] op_sel_hi:[1,0,1]
	v_pk_fma_f32 v[36:37], v[134:135], s[100:101], v[10:11] op_sel_hi:[1,0,1]
	v_min_f32_e32 v34, 0x40e00000, v34
	v_min_f32_e32 v35, 0x40e00000, v35
	v_min_f32_e32 v36, 0x40e00000, v36
	v_min_f32_e32 v37, 0x40e00000, v37
	v_pk_mul_f32 v[38:39], v[34:35], s[100:101] op_sel:[0,1] op_sel_hi:[1,1]
	v_pk_mul_f32 v[40:41], v[36:37], s[100:101] op_sel:[0,1] op_sel_hi:[1,1]
	v_exp_f32_e32 v38, v38
	v_exp_f32_e32 v39, v39
	v_exp_f32_e32 v40, v40
	v_exp_f32_e32 v41, v41
	v_pk_fma_f32 v[42:43], v[100:101], s[100:101], v[32:33] op_sel_hi:[1,0,1]
	v_pk_fma_f32 v[44:45], v[102:103], s[100:101], v[26:27] op_sel_hi:[1,0,1]
	v_pk_add_f32 v[38:39], v[38:39], 1.0 op_sel_hi:[1,0]
	v_pk_add_f32 v[40:41], v[40:41], 1.0 op_sel_hi:[1,0]
	v_rcp_f32_e32 v38, v38
	v_rcp_f32_e32 v39, v39
	v_rcp_f32_e32 v40, v40
	v_rcp_f32_e32 v41, v41
	v_med3_f32 v42, v42, s2, v250
	v_med3_f32 v43, v43, s2, v250
	v_med3_f32 v44, v44, s2, v250
	v_med3_f32 v45, v45, s2, v250
	v_pk_mul_f32 v[34:35], v[34:35], v[38:39]
	v_pk_mul_f32 v[36:37], v[36:37], v[40:41]
	v_pk_mul_f32 v[48:49], v[42:43], v[34:35]
	v_pk_mul_f32 v[50:51], v[44:45], v[36:37]
	v_pk_fma_f32 v[34:35], v[128:129], s[100:101], v[4:5] op_sel_hi:[1,0,1]
	v_pk_fma_f32 v[36:37], v[130:131], s[100:101], v[6:7] op_sel_hi:[1,0,1]
	v_min_f32_e32 v34, 0x40e00000, v34
	v_min_f32_e32 v35, 0x40e00000, v35
	v_min_f32_e32 v36, 0x40e00000, v36
	v_min_f32_e32 v37, 0x40e00000, v37
	v_pk_mul_f32 v[38:39], v[34:35], s[100:101] op_sel:[0,1] op_sel_hi:[1,1]
	v_pk_mul_f32 v[40:41], v[36:37], s[100:101] op_sel:[0,1] op_sel_hi:[1,1]
	v_exp_f32_e32 v38, v38
	v_exp_f32_e32 v39, v39
	v_exp_f32_e32 v40, v40
	v_exp_f32_e32 v41, v41
	v_pk_fma_f32 v[42:43], v[96:97], s[100:101], v[22:23] op_sel_hi:[1,0,1]
	v_pk_fma_f32 v[44:45], v[98:99], s[100:101], v[20:21] op_sel_hi:[1,0,1]
	v_pk_add_f32 v[38:39], v[38:39], 1.0 op_sel_hi:[1,0]
	v_pk_add_f32 v[40:41], v[40:41], 1.0 op_sel_hi:[1,0]
	v_rcp_f32_e32 v38, v38
	v_rcp_f32_e32 v39, v39
	v_rcp_f32_e32 v40, v40
	v_rcp_f32_e32 v41, v41
	v_med3_f32 v42, v42, s2, v250
	v_med3_f32 v43, v43, s2, v250
	v_med3_f32 v44, v44, s2, v250
	v_med3_f32 v45, v45, s2, v250
	v_pk_mul_f32 v[34:35], v[34:35], v[38:39]
	v_pk_mul_f32 v[36:37], v[36:37], v[40:41]
	v_pk_mul_f32 v[52:53], v[42:43], v[34:35]
	v_pk_mul_f32 v[54:55], v[44:45], v[36:37]
	v_cvt_pk_fp8_f32 v46, v48, v49
	v_cvt_pk_fp8_f32 v46, v50, v51 op_sel:[0,0,1]
	v_cvt_pk_fp8_f32 v47, v52, v53
	v_cvt_pk_fp8_f32 v47, v54, v55 op_sel:[0,0,1]
	ds_write_b64 v60, v[46:47]
	s_waitcnt lgkmcnt(0)
	s_barrier
	s_cmp_lg_u32 s98, 0
	s_cbranch_scc1 .Lupl_skip_4
	ds_read_b128 v[64:67], v61
	s_waitcnt lgkmcnt(0)
	global_store_dwordx4 v[56:57], v[64:67], off sc1
.Lupl_skip_4:
	v_lshl_add_u64 v[56:57], v[56:57], 0, s[0:1]
	v_pk_fma_f32 v[34:35], v[124:125], s[100:101], v[8:9] op_sel_hi:[1,0,1]
	v_pk_fma_f32 v[36:37], v[126:127], s[100:101], v[10:11] op_sel_hi:[1,0,1]
	v_min_f32_e32 v34, 0x40e00000, v34
	v_min_f32_e32 v35, 0x40e00000, v35
	v_min_f32_e32 v36, 0x40e00000, v36
	v_min_f32_e32 v37, 0x40e00000, v37
	v_pk_mul_f32 v[38:39], v[34:35], s[100:101] op_sel:[0,1] op_sel_hi:[1,1]
	v_pk_mul_f32 v[40:41], v[36:37], s[100:101] op_sel:[0,1] op_sel_hi:[1,1]
	v_exp_f32_e32 v38, v38
	v_exp_f32_e32 v39, v39
	v_exp_f32_e32 v40, v40
	v_exp_f32_e32 v41, v41
	v_pk_fma_f32 v[42:43], v[92:93], s[100:101], v[32:33] op_sel_hi:[1,0,1]
	v_pk_fma_f32 v[44:45], v[94:95], s[100:101], v[26:27] op_sel_hi:[1,0,1]
	v_pk_add_f32 v[38:39], v[38:39], 1.0 op_sel_hi:[1,0]
	v_pk_add_f32 v[40:41], v[40:41], 1.0 op_sel_hi:[1,0]
	v_rcp_f32_e32 v38, v38
	v_rcp_f32_e32 v39, v39
	v_rcp_f32_e32 v40, v40
	v_rcp_f32_e32 v41, v41
	v_med3_f32 v42, v42, s2, v250
	v_med3_f32 v43, v43, s2, v250
	v_med3_f32 v44, v44, s2, v250
	v_med3_f32 v45, v45, s2, v250
	v_pk_mul_f32 v[34:35], v[34:35], v[38:39]
	v_pk_mul_f32 v[36:37], v[36:37], v[40:41]
	v_pk_mul_f32 v[48:49], v[42:43], v[34:35]
	v_pk_mul_f32 v[50:51], v[44:45], v[36:37]
	v_pk_fma_f32 v[34:35], v[120:121], s[100:101], v[4:5] op_sel_hi:[1,0,1]
	v_pk_fma_f32 v[36:37], v[122:123], s[100:101], v[6:7] op_sel_hi:[1,0,1]
	v_min_f32_e32 v34, 0x40e00000, v34
	v_min_f32_e32 v35, 0x40e00000, v35
	v_min_f32_e32 v36, 0x40e00000, v36
	v_min_f32_e32 v37, 0x40e00000, v37
	v_pk_mul_f32 v[38:39], v[34:35], s[100:101] op_sel:[0,1] op_sel_hi:[1,1]
	v_pk_mul_f32 v[40:41], v[36:37], s[100:101] op_sel:[0,1] op_sel_hi:[1,1]
	v_exp_f32_e32 v38, v38
	v_exp_f32_e32 v39, v39
	v_exp_f32_e32 v40, v40
	v_exp_f32_e32 v41, v41
	v_pk_fma_f32 v[42:43], v[88:89], s[100:101], v[22:23] op_sel_hi:[1,0,1]
	v_pk_fma_f32 v[44:45], v[90:91], s[100:101], v[20:21] op_sel_hi:[1,0,1]
	v_pk_add_f32 v[38:39], v[38:39], 1.0 op_sel_hi:[1,0]
	v_pk_add_f32 v[40:41], v[40:41], 1.0 op_sel_hi:[1,0]
	v_rcp_f32_e32 v38, v38
	v_rcp_f32_e32 v39, v39
	v_rcp_f32_e32 v40, v40
	v_rcp_f32_e32 v41, v41
	v_med3_f32 v42, v42, s2, v250
	v_med3_f32 v43, v43, s2, v250
	v_med3_f32 v44, v44, s2, v250
	v_med3_f32 v45, v45, s2, v250
	v_pk_mul_f32 v[34:35], v[34:35], v[38:39]
	v_pk_mul_f32 v[36:37], v[36:37], v[40:41]
	v_pk_mul_f32 v[52:53], v[42:43], v[34:35]
	v_pk_mul_f32 v[54:55], v[44:45], v[36:37]
	v_cvt_pk_fp8_f32 v58, v48, v49
	v_cvt_pk_fp8_f32 v58, v50, v51 op_sel:[0,0,1]
	v_cvt_pk_fp8_f32 v59, v52, v53
	v_cvt_pk_fp8_f32 v59, v54, v55 op_sel:[0,0,1]
	ds_write_b64 v60, v[58:59] offset:4608
	s_waitcnt lgkmcnt(0)
	s_barrier
	s_cmp_lg_u32 s98, 1
	s_cbranch_scc1 .Lupl_skip_5
	ds_read_b128 v[64:67], v61 offset:4608
	s_waitcnt lgkmcnt(0)
	global_store_dwordx4 v[56:57], v[64:67], off sc1
.Lupl_skip_5:
	v_lshl_add_u64 v[56:57], v[56:57], 0, s[0:1]
	v_pk_fma_f32 v[34:35], v[116:117], s[100:101], v[8:9] op_sel_hi:[1,0,1]
	v_pk_fma_f32 v[36:37], v[118:119], s[100:101], v[10:11] op_sel_hi:[1,0,1]
	v_min_f32_e32 v34, 0x40e00000, v34
	v_min_f32_e32 v35, 0x40e00000, v35
	v_min_f32_e32 v36, 0x40e00000, v36
	v_min_f32_e32 v37, 0x40e00000, v37
	v_pk_mul_f32 v[38:39], v[34:35], s[100:101] op_sel:[0,1] op_sel_hi:[1,1]
	v_pk_mul_f32 v[40:41], v[36:37], s[100:101] op_sel:[0,1] op_sel_hi:[1,1]
	v_exp_f32_e32 v38, v38
	v_exp_f32_e32 v39, v39
	v_exp_f32_e32 v40, v40
	v_exp_f32_e32 v41, v41
	v_pk_fma_f32 v[42:43], v[84:85], s[100:101], v[32:33] op_sel_hi:[1,0,1]
	v_pk_fma_f32 v[44:45], v[86:87], s[100:101], v[26:27] op_sel_hi:[1,0,1]
	v_pk_add_f32 v[38:39], v[38:39], 1.0 op_sel_hi:[1,0]
	v_pk_add_f32 v[40:41], v[40:41], 1.0 op_sel_hi:[1,0]
	v_rcp_f32_e32 v38, v38
	v_rcp_f32_e32 v39, v39
	v_rcp_f32_e32 v40, v40
	v_rcp_f32_e32 v41, v41
	v_med3_f32 v42, v42, s2, v250
	v_med3_f32 v43, v43, s2, v250
	v_med3_f32 v44, v44, s2, v250
	v_med3_f32 v45, v45, s2, v250
	v_pk_mul_f32 v[34:35], v[34:35], v[38:39]
	v_pk_mul_f32 v[36:37], v[36:37], v[40:41]
	v_pk_mul_f32 v[48:49], v[42:43], v[34:35]
	v_pk_mul_f32 v[50:51], v[44:45], v[36:37]
	v_pk_fma_f32 v[34:35], v[112:113], s[100:101], v[4:5] op_sel_hi:[1,0,1]
	v_pk_fma_f32 v[36:37], v[114:115], s[100:101], v[6:7] op_sel_hi:[1,0,1]
	v_min_f32_e32 v34, 0x40e00000, v34
	v_min_f32_e32 v35, 0x40e00000, v35
	v_min_f32_e32 v36, 0x40e00000, v36
	v_min_f32_e32 v37, 0x40e00000, v37
	v_pk_mul_f32 v[38:39], v[34:35], s[100:101] op_sel:[0,1] op_sel_hi:[1,1]
	v_pk_mul_f32 v[40:41], v[36:37], s[100:101] op_sel:[0,1] op_sel_hi:[1,1]
	v_exp_f32_e32 v38, v38
	v_exp_f32_e32 v39, v39
	v_exp_f32_e32 v40, v40
	v_exp_f32_e32 v41, v41
	v_pk_fma_f32 v[42:43], v[80:81], s[100:101], v[22:23] op_sel_hi:[1,0,1]
	v_pk_fma_f32 v[44:45], v[82:83], s[100:101], v[20:21] op_sel_hi:[1,0,1]
	v_pk_add_f32 v[38:39], v[38:39], 1.0 op_sel_hi:[1,0]
	v_pk_add_f32 v[40:41], v[40:41], 1.0 op_sel_hi:[1,0]
	v_rcp_f32_e32 v38, v38
	v_rcp_f32_e32 v39, v39
	v_rcp_f32_e32 v40, v40
	v_rcp_f32_e32 v41, v41
	v_med3_f32 v42, v42, s2, v250
	v_med3_f32 v43, v43, s2, v250
	v_med3_f32 v44, v44, s2, v250
	v_med3_f32 v45, v45, s2, v250
	v_pk_mul_f32 v[34:35], v[34:35], v[38:39]
	v_pk_mul_f32 v[36:37], v[36:37], v[40:41]
	v_pk_mul_f32 v[52:53], v[42:43], v[34:35]
	v_pk_mul_f32 v[54:55], v[44:45], v[36:37]
	v_cvt_pk_fp8_f32 v46, v48, v49
	v_cvt_pk_fp8_f32 v46, v50, v51 op_sel:[0,0,1]
	v_cvt_pk_fp8_f32 v47, v52, v53
	v_cvt_pk_fp8_f32 v47, v54, v55 op_sel:[0,0,1]
	ds_write_b64 v60, v[46:47]
	s_waitcnt lgkmcnt(0)
	s_barrier
	s_cmp_lg_u32 s98, 0
	s_cbranch_scc1 .Lupl_skip_6
	ds_read_b128 v[64:67], v61
	s_waitcnt lgkmcnt(0)
	global_store_dwordx4 v[56:57], v[64:67], off sc1
.Lupl_skip_6:
	v_lshl_add_u64 v[56:57], v[56:57], 0, s[0:1]
	v_pk_fma_f32 v[34:35], v[108:109], s[100:101], v[8:9] op_sel_hi:[1,0,1]
	v_pk_fma_f32 v[36:37], v[110:111], s[100:101], v[10:11] op_sel_hi:[1,0,1]
	v_min_f32_e32 v34, 0x40e00000, v34
	v_min_f32_e32 v35, 0x40e00000, v35
	v_min_f32_e32 v36, 0x40e00000, v36
	v_min_f32_e32 v37, 0x40e00000, v37
	v_pk_mul_f32 v[38:39], v[34:35], s[100:101] op_sel:[0,1] op_sel_hi:[1,1]
	v_pk_mul_f32 v[40:41], v[36:37], s[100:101] op_sel:[0,1] op_sel_hi:[1,1]
	v_exp_f32_e32 v38, v38
	v_exp_f32_e32 v39, v39
	v_exp_f32_e32 v40, v40
	v_exp_f32_e32 v41, v41
	v_pk_fma_f32 v[42:43], v[76:77], s[100:101], v[32:33] op_sel_hi:[1,0,1]
	v_pk_fma_f32 v[44:45], v[78:79], s[100:101], v[26:27] op_sel_hi:[1,0,1]
	v_pk_add_f32 v[38:39], v[38:39], 1.0 op_sel_hi:[1,0]
	v_pk_add_f32 v[40:41], v[40:41], 1.0 op_sel_hi:[1,0]
	v_rcp_f32_e32 v38, v38
	v_rcp_f32_e32 v39, v39
	v_rcp_f32_e32 v40, v40
	v_rcp_f32_e32 v41, v41
	v_med3_f32 v42, v42, s2, v250
	v_med3_f32 v43, v43, s2, v250
	v_med3_f32 v44, v44, s2, v250
	v_med3_f32 v45, v45, s2, v250
	v_pk_mul_f32 v[34:35], v[34:35], v[38:39]
	v_pk_mul_f32 v[36:37], v[36:37], v[40:41]
	v_pk_mul_f32 v[48:49], v[42:43], v[34:35]
	v_pk_mul_f32 v[50:51], v[44:45], v[36:37]
	v_pk_fma_f32 v[34:35], v[104:105], s[100:101], v[4:5] op_sel_hi:[1,0,1]
	v_pk_fma_f32 v[36:37], v[106:107], s[100:101], v[6:7] op_sel_hi:[1,0,1]
	v_min_f32_e32 v34, 0x40e00000, v34
	v_min_f32_e32 v35, 0x40e00000, v35
	v_min_f32_e32 v36, 0x40e00000, v36
	v_min_f32_e32 v37, 0x40e00000, v37
	v_pk_mul_f32 v[38:39], v[34:35], s[100:101] op_sel:[0,1] op_sel_hi:[1,1]
	v_pk_mul_f32 v[40:41], v[36:37], s[100:101] op_sel:[0,1] op_sel_hi:[1,1]
	v_exp_f32_e32 v38, v38
	v_exp_f32_e32 v39, v39
	v_exp_f32_e32 v40, v40
	v_exp_f32_e32 v41, v41
	v_pk_fma_f32 v[42:43], v[12:13], s[100:101], v[22:23] op_sel_hi:[1,0,1]
	v_pk_fma_f32 v[44:45], v[14:15], s[100:101], v[20:21] op_sel_hi:[1,0,1]
	v_pk_add_f32 v[38:39], v[38:39], 1.0 op_sel_hi:[1,0]
	v_pk_add_f32 v[40:41], v[40:41], 1.0 op_sel_hi:[1,0]
	v_rcp_f32_e32 v38, v38
	v_rcp_f32_e32 v39, v39
	v_rcp_f32_e32 v40, v40
	v_rcp_f32_e32 v41, v41
	v_med3_f32 v42, v42, s2, v250
	v_med3_f32 v43, v43, s2, v250
	v_med3_f32 v44, v44, s2, v250
	v_med3_f32 v45, v45, s2, v250
	v_pk_mul_f32 v[34:35], v[34:35], v[38:39]
	v_pk_mul_f32 v[36:37], v[36:37], v[40:41]
	v_pk_mul_f32 v[52:53], v[42:43], v[34:35]
	v_pk_mul_f32 v[54:55], v[44:45], v[36:37]
	v_cvt_pk_fp8_f32 v58, v48, v49
	v_cvt_pk_fp8_f32 v58, v50, v51 op_sel:[0,0,1]
	v_cvt_pk_fp8_f32 v59, v52, v53
	v_cvt_pk_fp8_f32 v59, v54, v55 op_sel:[0,0,1]
	ds_write_b64 v60, v[58:59] offset:4608
	s_waitcnt lgkmcnt(0)
	s_barrier
	s_cmp_lg_u32 s98, 1
	s_cbranch_scc1 .Lupl_skip_7
	ds_read_b128 v[64:67], v61 offset:4608
	s_waitcnt lgkmcnt(0)
	global_store_dwordx4 v[56:57], v[64:67], off sc1
.Lupl_skip_7:
.LBB0_1946:
	s_andn2_b64 vcc, exec, s[42:43]
	s_cbranch_vccnz .LBB0_1890
	s_andn2_b64 vcc, exec, s[20:21]
	s_cbranch_vccnz .LBB0_1889
	s_barrier
	s_branch .LBB0_1889
